# v048 + GEMM loop top: 16 bias ds_reads hoisted above the barrier and addressed from one base with immediate offsets (15 fewer VALU per item)
# speedup vs baseline: 1.0086x; 1.0071x over previous
.LBB3_142:
	s_lshl_b32 s2, s41, 5
	s_add_i32 s2, s2, s22
	s_xor_b64 s[18:19], s[20:21], -1
	s_lshr_b32 s20, s2, 3
	v_mov_b32_e32 v210, v0
	s_add_i32 s20, s20, s24
	s_add_i32 s2, s20, s25
	v_ashrrev_i32_e32 v212, 6, v210
	v_lshl_add_u32 v2, s2, 3, v212
	v_ashrrev_i32_e32 v3, 31, v2
	v_and_b32_e32 v213, 63, v210
	v_lshlrev_b64 v[2:3], 15, v[2:3]
	v_lshl_add_u64 v[2:3], s[10:11], 0, v[2:3]
	v_lshlrev_b32_e32 v206, 4, v213
	v_lshl_add_u64 v[204:205], v[2:3], 0, v[206:207]
	v_and_b32_e32 v2, 3, v212
	v_lshlrev_b32_e32 v3, 3, v212
	v_and_or_b32 v214, v3, 32, v2
	v_and_b32_e32 v2, 0x3fffff8, v212
	v_add_u32_e32 v4, 8, v212
	v_or_b32_e32 v2, s23, v2
	v_and_b32_e32 v4, 0x3fffff8, v4
	v_or_b32_e32 v6, 8, v214
	v_lshlrev_b32_e32 v215, 6, v2
	v_or_b32_e32 v4, s23, v4
	v_or_b32_e32 v2, v6, v215
	v_lshlrev_b32_e32 v216, 6, v4
	v_lshlrev_b32_e32 v209, 10, v212
	v_ashrrev_i32_e32 v3, 31, v2
	v_or_b32_e32 v4, v216, v6
	v_or_b32_e32 v208, v206, v209
	v_lshl_add_u64 v[202:203], s[0:1], 0, v[206:207]
	v_lshlrev_b64 v[2:3], 10, v[2:3]
	v_ashrrev_i32_e32 v5, 31, v4
	s_waitcnt vmcnt(17)
	ds_write_b128 v208, v[190:193]
	s_waitcnt vmcnt(16)
	ds_write_b128 v208, v[194:197] offset:8192
	s_waitcnt vmcnt(15)
	ds_write_b128 v208, v[198:201] offset:16384
	v_lshl_add_u64 v[2:3], v[202:203], 0, v[2:3]
	v_lshlrev_b64 v[4:5], 10, v[4:5]
	v_lshl_add_u64 v[4:5], v[202:203], 0, v[4:5]
	global_load_dwordx4 v[98:101], v[2:3], off
	global_load_dwordx4 v[102:105], v[4:5], off
	v_add_u32_e32 v2, 16, v212
	v_and_b32_e32 v2, 0x3fffff8, v2
	v_or_b32_e32 v2, s23, v2
	v_lshlrev_b32_e32 v217, 6, v2
	v_or_b32_e32 v2, v217, v6
	v_ashrrev_i32_e32 v3, 31, v2
	v_lshlrev_b64 v[2:3], 10, v[2:3]
	v_lshl_add_u64 v[2:3], v[202:203], 0, v[2:3]
	global_load_dwordx4 v[106:109], v[2:3], off
	v_lshrrev_b32_e32 v2, 3, v210
	v_or_b32_e32 v10, 12, v214
	v_and_b32_e32 v211, 4, v2
	v_or_b32_e32 v2, v10, v215
	v_ashrrev_i32_e32 v3, 31, v2
	v_or_b32_e32 v4, v10, v216
	v_lshlrev_b64 v[2:3], 10, v[2:3]
	v_ashrrev_i32_e32 v5, 31, v4
	v_lshl_add_u64 v[2:3], v[202:203], 0, v[2:3]
	v_lshlrev_b64 v[4:5], 10, v[4:5]
	v_lshlrev_b32_e32 v8, 2, v211
	v_or_b32_e32 v8, 0x1e000, v8
	ds_read_b128 v[50:53], v8
	ds_read_b128 v[54:57], v8 offset:32
	ds_read_b128 v[58:61], v8 offset:64
	ds_read_b128 v[62:65], v8 offset:96
	ds_read_b128 v[18:21], v8 offset:128
	ds_read_b128 v[22:25], v8 offset:160
	ds_read_b128 v[26:29], v8 offset:192
	ds_read_b128 v[30:33], v8 offset:224
	ds_read_b128 v[82:85], v8 offset:256
	ds_read_b128 v[86:89], v8 offset:288
	ds_read_b128 v[90:93], v8 offset:320
	ds_read_b128 v[94:97], v8 offset:352
	ds_read_b128 v[34:37], v8 offset:384
	ds_read_b128 v[38:41], v8 offset:416
	ds_read_b128 v[42:45], v8 offset:448
	ds_read_b128 v[46:49], v8 offset:480
	s_waitcnt lgkmcnt(0)
	s_barrier
	v_lshl_add_u64 v[4:5], v[202:203], 0, v[4:5]
	global_load_dwordx4 v[118:121], v[2:3], off
	global_load_dwordx4 v[122:125], v[4:5], off
	v_or_b32_e32 v2, v10, v217
	v_ashrrev_i32_e32 v3, 31, v2
	v_lshlrev_b64 v[2:3], 10, v[2:3]
	v_lshl_add_u64 v[2:3], v[202:203], 0, v[2:3]
	global_load_dwordx4 v[190:193], v[2:3], off
	v_and_b32_e32 v1, 31, v210
	v_lshlrev_b32_e32 v6, 2, v1
	v_or_b32_e32 v4, 0x1e200, v6
	ds_read_b32 v66, v4
	v_or_b32_e32 v2, 0x1e280, v6
	ds_read_b32 v2, v2
	ds_read_b128 v[110:113], v206
	ds_read_b128 v[114:117], v206 offset:4096
	ds_read_b128 v[126:129], v206 offset:8192
	ds_read_b128 v[194:197], v206 offset:12288
	ds_read_b128 v[198:201], v206 offset:16384
	ds_read_b128 v[218:221], v206 offset:20480
	s_waitcnt vmcnt(20)
	ds_write_b128 v208, v[174:177] offset:24576
	s_waitcnt vmcnt(19)
	ds_write_b128 v208, v[182:185] offset:32768
	s_waitcnt vmcnt(18)
	ds_write_b128 v208, v[186:189] offset:40960
	ds_read_b128 v[174:177], v206 offset:1024
	ds_read_b128 v[182:185], v206 offset:5120
	ds_read_b128 v[186:189], v206 offset:9216
	ds_read_b128 v[222:225], v206 offset:13312
	ds_read_b128 v[226:229], v206 offset:17408
	ds_read_b128 v[230:233], v206 offset:21504
	s_waitcnt lgkmcnt(14)
	v_mov_b32_e32 v67, v66
	v_mov_b32_e32 v68, v66
	v_mov_b32_e32 v69, v66
	v_mov_b32_e32 v70, v66
	v_mov_b32_e32 v71, v66
	v_mov_b32_e32 v72, v66
	v_mov_b32_e32 v73, v66
	v_mov_b32_e32 v74, v66
	v_mov_b32_e32 v75, v66
	v_mov_b32_e32 v76, v66
	v_mov_b32_e32 v77, v66
	v_mov_b32_e32 v78, v66
	v_mov_b32_e32 v79, v66
	v_mov_b32_e32 v80, v66
	v_mov_b32_e32 v81, v66
	v_mov_b32_e32 v3, v2
	v_mov_b32_e32 v4, v2
	v_mov_b32_e32 v5, v2
	v_mov_b32_e32 v6, v2
	v_mov_b32_e32 v7, v2
	v_mov_b32_e32 v8, v2
	v_mov_b32_e32 v9, v2
	v_mov_b32_e32 v10, v2
	v_mov_b32_e32 v11, v2
	v_mov_b32_e32 v12, v2
	v_mov_b32_e32 v13, v2
	v_mov_b32_e32 v14, v2
	v_mov_b32_e32 v15, v2
	v_mov_b32_e32 v16, v2
	v_mov_b32_e32 v17, v2
	s_waitcnt vmcnt(17)
	v_mfma_f32_32x32x16_bf16 v[50:65], v[110:113], v[170:173], v[50:65]
	s_waitcnt lgkmcnt(13)
	v_mfma_f32_32x32x16_bf16 v[18:33], v[114:117], v[170:173], v[18:33]
	s_waitcnt lgkmcnt(12)
	v_mfma_f32_32x32x16_bf16 v[82:97], v[126:129], v[170:173], v[82:97]
	s_waitcnt lgkmcnt(11)
	v_mfma_f32_32x32x16_bf16 v[34:49], v[194:197], v[170:173], v[34:49]
	s_waitcnt lgkmcnt(10)
	v_mfma_f32_32x32x16_bf16 v[66:81], v[170:173], v[198:201], v[66:81]
	s_waitcnt lgkmcnt(9)
	v_mfma_f32_32x32x16_bf16 v[2:17], v[170:173], v[218:221], v[2:17]
	ds_read_b128 v[110:113], v206 offset:2048
	ds_read_b128 v[114:117], v206 offset:6144
	ds_read_b128 v[126:129], v206 offset:10240
	ds_read_b128 v[170:173], v206 offset:14336
	ds_read_b128 v[194:197], v206 offset:18432
	ds_read_b128 v[198:201], v206 offset:22528
	s_waitcnt vmcnt(16) lgkmcnt(11)
	v_mfma_f32_32x32x16_bf16 v[50:65], v[174:177], v[162:165], v[50:65]
	s_waitcnt lgkmcnt(10)
	v_mfma_f32_32x32x16_bf16 v[18:33], v[182:185], v[162:165], v[18:33]
	s_waitcnt lgkmcnt(9)
	v_mfma_f32_32x32x16_bf16 v[82:97], v[186:189], v[162:165], v[82:97]
	s_waitcnt lgkmcnt(8)
	v_mfma_f32_32x32x16_bf16 v[34:49], v[222:225], v[162:165], v[34:49]
	s_waitcnt lgkmcnt(7)
	v_mfma_f32_32x32x16_bf16 v[66:81], v[162:165], v[226:229], v[66:81]
	s_waitcnt lgkmcnt(6)
	v_mfma_f32_32x32x16_bf16 v[2:17], v[162:165], v[230:233], v[2:17]
	s_waitcnt lgkmcnt(6)
	s_barrier
	ds_read_b128 v[162:165], v206 offset:3072
	ds_read_b128 v[174:177], v206 offset:7168
	ds_read_b128 v[182:185], v206 offset:11264
	ds_read_b128 v[186:189], v206 offset:15360
	ds_read_b128 v[218:221], v206 offset:19456
	ds_read_b128 v[222:225], v206 offset:23552
	s_waitcnt vmcnt(15) lgkmcnt(11)
	v_mfma_f32_32x32x16_bf16 v[50:65], v[110:113], v[154:157], v[50:65]
	s_waitcnt lgkmcnt(10)
	v_mfma_f32_32x32x16_bf16 v[18:33], v[114:117], v[154:157], v[18:33]
	s_waitcnt lgkmcnt(9)
	v_mfma_f32_32x32x16_bf16 v[82:97], v[126:129], v[154:157], v[82:97]
	s_waitcnt lgkmcnt(8)
	v_mfma_f32_32x32x16_bf16 v[34:49], v[170:173], v[154:157], v[34:49]
	s_waitcnt lgkmcnt(7)
	v_mfma_f32_32x32x16_bf16 v[66:81], v[154:157], v[194:197], v[66:81]
	s_waitcnt lgkmcnt(6)
	v_mfma_f32_32x32x16_bf16 v[2:17], v[154:157], v[198:201], v[2:17]
	ds_read_b128 v[194:197], v206 offset:24576
	ds_read_b128 v[198:201], v206 offset:28672
	ds_read_b128 v[226:229], v206 offset:32768
	ds_read_b128 v[230:233], v206 offset:36864
	ds_read_b128 v[234:237], v206 offset:40960
	ds_read_b128 v[238:241], v206 offset:45056
	v_add_co_u32_e32 v110, vcc, s29, v204
	s_waitcnt vmcnt(14) lgkmcnt(11)
	v_mfma_f32_32x32x16_bf16 v[50:65], v[162:165], v[146:149], v[50:65]
	v_addc_co_u32_e32 v111, vcc, 0, v205, vcc
	v_add_co_u32_e32 v242, vcc, s30, v204
	s_nop 1
	v_addc_co_u32_e32 v243, vcc, 0, v205, vcc
	global_load_dwordx4 v[126:129], v[110:111], off offset:1024
	global_load_dwordx4 v[114:117], v[110:111], off offset:2048
	global_load_dwordx4 v[154:157], v[242:243], off offset:-4096
	s_nop 0
	global_load_dwordx4 v[110:113], v[110:111], off offset:3072
	s_waitcnt lgkmcnt(10)
	v_mfma_f32_32x32x16_bf16 v[18:33], v[174:177], v[146:149], v[18:33]
	s_waitcnt lgkmcnt(9)
	v_mfma_f32_32x32x16_bf16 v[82:97], v[182:185], v[146:149], v[82:97]
	s_waitcnt lgkmcnt(8)
	v_mfma_f32_32x32x16_bf16 v[34:49], v[186:189], v[146:149], v[34:49]
	s_waitcnt lgkmcnt(7)
	v_mfma_f32_32x32x16_bf16 v[66:81], v[146:149], v[218:221], v[66:81]
	s_waitcnt lgkmcnt(6)
	v_mfma_f32_32x32x16_bf16 v[2:17], v[146:149], v[222:225], v[2:17]
	v_or_b32_e32 v170, 16, v214
	v_or_b32_e32 v146, v170, v215
	v_or_b32_e32 v148, v170, v216
	v_or_b32_e32 v170, v170, v217
	v_ashrrev_i32_e32 v147, 31, v146
	v_ashrrev_i32_e32 v149, 31, v148
	v_ashrrev_i32_e32 v171, 31, v170
	v_lshlrev_b64 v[146:147], 10, v[146:147]
	v_lshlrev_b64 v[148:149], 10, v[148:149]
	v_lshlrev_b64 v[170:171], 10, v[170:171]
	v_lshl_add_u64 v[146:147], v[202:203], 0, v[146:147]
	v_lshl_add_u64 v[162:163], v[202:203], 0, v[148:149]
	v_lshl_add_u64 v[170:171], v[202:203], 0, v[170:171]
	global_load_dwordx4 v[146:149], v[146:147], off
	s_nop 0
	global_load_dwordx4 v[162:165], v[162:163], off
	v_or_b32_e32 v244, 0x10000, v206
	global_load_dwordx4 v[170:173], v[170:171], off
	v_add_u32_e32 v209, v244, v209
	s_waitcnt vmcnt(12)
	ds_write_b128 v208, v[98:101] offset:49152
	s_waitcnt vmcnt(11)
	ds_write_b128 v208, v[102:105] offset:57344
	s_waitcnt vmcnt(10)
	ds_write_b128 v209, v[106:109]
	ds_read_b128 v[98:101], v206 offset:25600
	ds_read_b128 v[102:105], v206 offset:29696
	ds_read_b128 v[106:109], v206 offset:33792
	ds_read_b128 v[174:177], v206 offset:37888
	ds_read_b128 v[182:185], v206 offset:41984
	ds_read_b128 v[186:189], v206 offset:46080
	s_waitcnt lgkmcnt(14)
	v_mfma_f32_32x32x16_bf16 v[50:65], v[194:197], v[178:181], v[50:65]
	s_waitcnt lgkmcnt(13)
	v_mfma_f32_32x32x16_bf16 v[18:33], v[198:201], v[178:181], v[18:33]
	s_waitcnt lgkmcnt(12)
	v_mfma_f32_32x32x16_bf16 v[82:97], v[226:229], v[178:181], v[82:97]
	s_waitcnt lgkmcnt(11)
	v_mfma_f32_32x32x16_bf16 v[34:49], v[230:233], v[178:181], v[34:49]
	s_waitcnt lgkmcnt(10)
	v_mfma_f32_32x32x16_bf16 v[66:81], v[178:181], v[234:237], v[66:81]
	s_waitcnt lgkmcnt(9)
	v_mfma_f32_32x32x16_bf16 v[2:17], v[178:181], v[238:241], v[2:17]
	ds_read_b128 v[178:181], v206 offset:26624
	ds_read_b128 v[194:197], v206 offset:30720
	ds_read_b128 v[198:201], v206 offset:34816
	ds_read_b128 v[218:221], v206 offset:38912
	ds_read_b128 v[222:225], v206 offset:43008
	ds_read_b128 v[226:229], v206 offset:47104
	s_waitcnt lgkmcnt(11)
	v_mfma_f32_32x32x16_bf16 v[50:65], v[98:101], v[166:169], v[50:65]
	s_waitcnt lgkmcnt(10)
	v_mfma_f32_32x32x16_bf16 v[18:33], v[102:105], v[166:169], v[18:33]
	s_waitcnt lgkmcnt(9)
	v_mfma_f32_32x32x16_bf16 v[82:97], v[106:109], v[166:169], v[82:97]
	s_waitcnt lgkmcnt(8)
	v_mfma_f32_32x32x16_bf16 v[34:49], v[174:177], v[166:169], v[34:49]
	s_waitcnt lgkmcnt(7)
	v_mfma_f32_32x32x16_bf16 v[66:81], v[166:169], v[182:185], v[66:81]
	s_waitcnt lgkmcnt(6)
	v_mfma_f32_32x32x16_bf16 v[2:17], v[166:169], v[186:189], v[2:17]
	s_waitcnt lgkmcnt(6)
	s_barrier
	ds_read_b128 v[98:101], v206 offset:27648
	ds_read_b128 v[102:105], v206 offset:31744
	ds_read_b128 v[106:109], v206 offset:35840
	ds_read_b128 v[166:169], v206 offset:39936
	ds_read_b128 v[174:177], v206 offset:44032
	ds_read_b128 v[182:185], v206 offset:48128
	s_waitcnt lgkmcnt(11)
	v_mfma_f32_32x32x16_bf16 v[50:65], v[178:181], v[158:161], v[50:65]
	s_waitcnt lgkmcnt(10)
	v_mfma_f32_32x32x16_bf16 v[18:33], v[194:197], v[158:161], v[18:33]
	s_waitcnt lgkmcnt(9)
	v_mfma_f32_32x32x16_bf16 v[82:97], v[198:201], v[158:161], v[82:97]
	s_waitcnt lgkmcnt(8)
	v_mfma_f32_32x32x16_bf16 v[34:49], v[218:221], v[158:161], v[34:49]
	s_waitcnt lgkmcnt(7)
	v_mfma_f32_32x32x16_bf16 v[66:81], v[158:161], v[222:225], v[66:81]
	s_waitcnt lgkmcnt(6)
	v_mfma_f32_32x32x16_bf16 v[2:17], v[158:161], v[226:229], v[2:17]
	ds_read_b128 v[186:189], v206 offset:49152
	ds_read_b128 v[194:197], v206 offset:53248
	ds_read_b128 v[198:201], v206 offset:57344
	ds_read_b128 v[218:221], v206 offset:61440
	v_or_b32_e32 v240, 0x11000, v206
	ds_read_b128 v[222:225], v244
	ds_read_b128 v[226:229], v240
	s_waitcnt lgkmcnt(11)
	v_mfma_f32_32x32x16_bf16 v[50:65], v[98:101], v[150:153], v[50:65]
	s_waitcnt lgkmcnt(10)
	v_mfma_f32_32x32x16_bf16 v[18:33], v[102:105], v[150:153], v[18:33]
	s_waitcnt lgkmcnt(9)
	v_mfma_f32_32x32x16_bf16 v[82:97], v[106:109], v[150:153], v[82:97]
	global_load_dwordx4 v[158:161], v[242:243], off
	global_load_dwordx4 v[106:109], v[242:243], off offset:1024
	global_load_dwordx4 v[102:105], v[242:243], off offset:2048
	global_load_dwordx4 v[98:101], v[242:243], off offset:3072
	s_waitcnt lgkmcnt(8)
	v_mfma_f32_32x32x16_bf16 v[34:49], v[166:169], v[150:153], v[34:49]
	s_waitcnt lgkmcnt(7)
	v_mfma_f32_32x32x16_bf16 v[66:81], v[150:153], v[174:177], v[66:81]
	s_waitcnt lgkmcnt(6)
	v_mfma_f32_32x32x16_bf16 v[2:17], v[150:153], v[182:185], v[2:17]
	v_or_b32_e32 v174, 20, v214
	v_or_b32_e32 v150, v174, v215
	v_or_b32_e32 v152, v174, v216
	v_or_b32_e32 v174, v174, v217
	v_ashrrev_i32_e32 v151, 31, v150
	v_ashrrev_i32_e32 v153, 31, v152
	v_ashrrev_i32_e32 v175, 31, v174
	v_lshlrev_b64 v[150:151], 10, v[150:151]
	v_lshlrev_b64 v[152:153], 10, v[152:153]
	v_lshlrev_b64 v[174:175], 10, v[174:175]
	v_lshl_add_u64 v[150:151], v[202:203], 0, v[150:151]
	v_lshl_add_u64 v[166:167], v[202:203], 0, v[152:153]
	v_lshl_add_u64 v[174:175], v[202:203], 0, v[174:175]
	global_load_dwordx4 v[150:153], v[150:151], off
	s_nop 0
	global_load_dwordx4 v[166:169], v[166:167], off
	v_or_b32_e32 v241, 0x10400, v206
	global_load_dwordx4 v[178:181], v[174:175], off
	s_waitcnt vmcnt(16)
	ds_write_b128 v208, v[118:121]
	s_waitcnt vmcnt(15)
	ds_write_b128 v208, v[122:125] offset:8192
	s_waitcnt vmcnt(14)
	ds_write_b128 v208, v[190:193] offset:16384
	ds_read_b128 v[118:121], v206 offset:50176
	ds_read_b128 v[122:125], v206 offset:54272
	ds_read_b128 v[174:177], v206 offset:58368
	ds_read_b128 v[182:185], v206 offset:62464
	v_or_b32_e32 v242, 0x11400, v206
	ds_read_b128 v[190:193], v241
	ds_read_b128 v[230:233], v242
	s_waitcnt lgkmcnt(14)
	v_mfma_f32_32x32x16_bf16 v[50:65], v[186:189], v[142:145], v[50:65]
	s_waitcnt lgkmcnt(13)
	v_mfma_f32_32x32x16_bf16 v[18:33], v[194:197], v[142:145], v[18:33]
	s_waitcnt lgkmcnt(12)
	v_mfma_f32_32x32x16_bf16 v[82:97], v[198:201], v[142:145], v[82:97]
	s_waitcnt lgkmcnt(11)
	v_mfma_f32_32x32x16_bf16 v[34:49], v[218:221], v[142:145], v[34:49]
	s_waitcnt lgkmcnt(10)
	v_mfma_f32_32x32x16_bf16 v[66:81], v[142:145], v[222:225], v[66:81]
	s_waitcnt lgkmcnt(9)
	v_mfma_f32_32x32x16_bf16 v[2:17], v[142:145], v[226:229], v[2:17]
	ds_read_b128 v[142:145], v206 offset:51200
	ds_read_b128 v[186:189], v206 offset:55296
	ds_read_b128 v[194:197], v206 offset:59392
	ds_read_b128 v[198:201], v206 offset:63488
	v_or_b32_e32 v243, 0x10800, v206
	v_or_b32_e32 v245, 0x11800, v206
	ds_read_b128 v[218:221], v243
	ds_read_b128 v[222:225], v245
	s_waitcnt lgkmcnt(11)
	v_mfma_f32_32x32x16_bf16 v[50:65], v[118:121], v[138:141], v[50:65]
	s_waitcnt lgkmcnt(10)
	v_mfma_f32_32x32x16_bf16 v[18:33], v[122:125], v[138:141], v[18:33]
	s_waitcnt lgkmcnt(9)
	v_mfma_f32_32x32x16_bf16 v[82:97], v[174:177], v[138:141], v[82:97]
	s_waitcnt lgkmcnt(8)
	v_mfma_f32_32x32x16_bf16 v[34:49], v[182:185], v[138:141], v[34:49]
	s_waitcnt lgkmcnt(7)
	v_mfma_f32_32x32x16_bf16 v[66:81], v[138:141], v[190:193], v[66:81]
	s_waitcnt lgkmcnt(6)
	v_mfma_f32_32x32x16_bf16 v[2:17], v[138:141], v[230:233], v[2:17]
	s_waitcnt lgkmcnt(6)
	s_barrier
	ds_read_b128 v[118:121], v206 offset:52224
	ds_read_b128 v[122:125], v206 offset:56320
	ds_read_b128 v[138:141], v206 offset:60416
	ds_read_b128 v[174:177], v206 offset:64512
	v_or_b32_e32 v246, 0x10c00, v206
	v_or_b32_e32 v247, 0x11c00, v206
	ds_read_b128 v[182:185], v246
	ds_read_b128 v[190:193], v247
	s_waitcnt lgkmcnt(11)
	v_mfma_f32_32x32x16_bf16 v[50:65], v[142:145], v[134:137], v[50:65]
	s_waitcnt lgkmcnt(10)
	v_mfma_f32_32x32x16_bf16 v[18:33], v[186:189], v[134:137], v[18:33]
	s_waitcnt lgkmcnt(9)
	v_mfma_f32_32x32x16_bf16 v[82:97], v[194:197], v[134:137], v[82:97]
	s_waitcnt lgkmcnt(8)
	v_mfma_f32_32x32x16_bf16 v[34:49], v[198:201], v[134:137], v[34:49]
	s_waitcnt lgkmcnt(7)
	v_mfma_f32_32x32x16_bf16 v[66:81], v[134:137], v[218:221], v[66:81]
	s_waitcnt lgkmcnt(6)
	v_mfma_f32_32x32x16_bf16 v[2:17], v[134:137], v[222:225], v[2:17]
	ds_read_b128 v[186:189], v206
	ds_read_b128 v[218:221], v206 offset:4096
	ds_read_b128 v[222:225], v206 offset:8192
	ds_read_b128 v[226:229], v206 offset:12288
	ds_read_b128 v[230:233], v206 offset:16384
	ds_read_b128 v[234:237], v206 offset:20480
	s_waitcnt lgkmcnt(11)
	v_mfma_f32_32x32x16_bf16 v[50:65], v[118:121], v[130:133], v[50:65]
	v_add_co_u32_e32 v118, vcc, s31, v204
	s_nop 1
	v_addc_co_u32_e32 v119, vcc, 0, v205, vcc
	v_add_co_u32_e32 v238, vcc, s27, v204
	s_waitcnt lgkmcnt(10)
	v_mfma_f32_32x32x16_bf16 v[18:33], v[122:125], v[130:133], v[18:33]
	v_addc_co_u32_e32 v239, vcc, 0, v205, vcc
	s_waitcnt lgkmcnt(9)
	v_mfma_f32_32x32x16_bf16 v[82:97], v[138:141], v[130:133], v[82:97]
	global_load_dwordx4 v[138:141], v[118:119], off offset:1024
	global_load_dwordx4 v[134:137], v[118:119], off offset:2048
	s_waitcnt lgkmcnt(8)
	v_mfma_f32_32x32x16_bf16 v[34:49], v[174:177], v[130:133], v[34:49]
	s_waitcnt lgkmcnt(7)
	v_mfma_f32_32x32x16_bf16 v[66:81], v[130:133], v[182:185], v[66:81]
	s_waitcnt lgkmcnt(6)
	v_mfma_f32_32x32x16_bf16 v[2:17], v[130:133], v[190:193], v[2:17]
	global_load_dwordx4 v[142:145], v[238:239], off offset:-4096
	global_load_dwordx4 v[130:133], v[118:119], off offset:3072
	v_or_b32_e32 v122, 24, v214
	v_or_b32_e32 v118, v122, v215
	v_ashrrev_i32_e32 v119, 31, v118
	v_or_b32_e32 v120, v122, v216
	v_lshlrev_b64 v[118:119], 10, v[118:119]
	v_ashrrev_i32_e32 v121, 31, v120
	v_lshl_add_u64 v[118:119], v[202:203], 0, v[118:119]
	v_lshlrev_b64 v[120:121], 10, v[120:121]
	v_lshl_add_u64 v[120:121], v[202:203], 0, v[120:121]
	global_load_dwordx4 v[190:193], v[118:119], off
	global_load_dwordx4 v[194:197], v[120:121], off
	v_or_b32_e32 v118, v122, v217
	v_ashrrev_i32_e32 v119, 31, v118
	v_lshlrev_b64 v[118:119], 10, v[118:119]
	v_lshl_add_u64 v[118:119], v[202:203], 0, v[118:119]
	global_load_dwordx4 v[198:201], v[118:119], off
	s_waitcnt vmcnt(16)
	ds_write_b128 v208, v[146:149] offset:24576
	s_waitcnt vmcnt(15)
	ds_write_b128 v208, v[162:165] offset:32768
	s_waitcnt vmcnt(14)
	ds_write_b128 v208, v[170:173] offset:40960
	ds_read_b128 v[118:121], v206 offset:1024
	ds_read_b128 v[122:125], v206 offset:5120
	ds_read_b128 v[146:149], v206 offset:9216
	ds_read_b128 v[162:165], v206 offset:13312
	ds_read_b128 v[170:173], v206 offset:17408
	ds_read_b128 v[174:177], v206 offset:21504
	s_waitcnt lgkmcnt(14)
	v_mfma_f32_32x32x16_bf16 v[50:65], v[186:189], v[154:157], v[50:65]
	s_waitcnt lgkmcnt(13)
	v_mfma_f32_32x32x16_bf16 v[18:33], v[218:221], v[154:157], v[18:33]
	s_waitcnt lgkmcnt(12)
	v_mfma_f32_32x32x16_bf16 v[82:97], v[222:225], v[154:157], v[82:97]
	s_waitcnt lgkmcnt(11)
	v_mfma_f32_32x32x16_bf16 v[34:49], v[226:229], v[154:157], v[34:49]
	s_waitcnt lgkmcnt(10)
	v_mfma_f32_32x32x16_bf16 v[66:81], v[154:157], v[230:233], v[66:81]
	s_waitcnt lgkmcnt(9)
	v_mfma_f32_32x32x16_bf16 v[2:17], v[154:157], v[234:237], v[2:17]
	ds_read_b128 v[154:157], v206 offset:2048
	ds_read_b128 v[182:185], v206 offset:6144
	ds_read_b128 v[186:189], v206 offset:10240
	ds_read_b128 v[218:221], v206 offset:14336
	ds_read_b128 v[222:225], v206 offset:18432
	ds_read_b128 v[226:229], v206 offset:22528
	s_waitcnt lgkmcnt(11)
	v_mfma_f32_32x32x16_bf16 v[50:65], v[118:121], v[126:129], v[50:65]
	s_waitcnt lgkmcnt(10)
	v_mfma_f32_32x32x16_bf16 v[18:33], v[122:125], v[126:129], v[18:33]
	s_waitcnt lgkmcnt(9)
	v_mfma_f32_32x32x16_bf16 v[82:97], v[146:149], v[126:129], v[82:97]
	s_waitcnt lgkmcnt(8)
	v_mfma_f32_32x32x16_bf16 v[34:49], v[162:165], v[126:129], v[34:49]
	s_waitcnt lgkmcnt(7)
	v_mfma_f32_32x32x16_bf16 v[66:81], v[126:129], v[170:173], v[66:81]
	s_waitcnt lgkmcnt(6)
	v_mfma_f32_32x32x16_bf16 v[2:17], v[126:129], v[174:177], v[2:17]
	s_waitcnt lgkmcnt(6)
	s_barrier
	ds_read_b128 v[118:121], v206 offset:3072
	ds_read_b128 v[122:125], v206 offset:7168
	ds_read_b128 v[126:129], v206 offset:11264
	ds_read_b128 v[146:149], v206 offset:15360
	ds_read_b128 v[162:165], v206 offset:19456
	ds_read_b128 v[174:177], v206 offset:23552
	s_waitcnt lgkmcnt(11)
	v_mfma_f32_32x32x16_bf16 v[50:65], v[154:157], v[114:117], v[50:65]
	s_waitcnt lgkmcnt(10)
	v_mfma_f32_32x32x16_bf16 v[18:33], v[182:185], v[114:117], v[18:33]
	s_waitcnt lgkmcnt(9)
	v_mfma_f32_32x32x16_bf16 v[82:97], v[186:189], v[114:117], v[82:97]
	s_waitcnt lgkmcnt(8)
	v_mfma_f32_32x32x16_bf16 v[34:49], v[218:221], v[114:117], v[34:49]
	s_waitcnt lgkmcnt(7)
	v_mfma_f32_32x32x16_bf16 v[66:81], v[114:117], v[222:225], v[66:81]
	s_waitcnt lgkmcnt(6)
	v_mfma_f32_32x32x16_bf16 v[2:17], v[114:117], v[226:229], v[2:17]
	ds_read_b128 v[114:117], v206 offset:24576
	ds_read_b128 v[218:221], v206 offset:28672
	ds_read_b128 v[222:225], v206 offset:32768
	ds_read_b128 v[226:229], v206 offset:36864
	ds_read_b128 v[230:233], v206 offset:40960
	ds_read_b128 v[234:237], v206 offset:45056
	s_waitcnt lgkmcnt(8)
	v_mfma_f32_32x32x16_bf16 v[34:49], v[146:149], v[110:113], v[34:49]
	s_waitcnt lgkmcnt(7)
	v_mfma_f32_32x32x16_bf16 v[66:81], v[110:113], v[162:165], v[66:81]
	global_load_dwordx4 v[170:173], v[238:239], off
	global_load_dwordx4 v[162:165], v[238:239], off offset:1024
	global_load_dwordx4 v[154:157], v[238:239], off offset:2048
	global_load_dwordx4 v[146:149], v[238:239], off offset:3072
	v_mfma_f32_32x32x16_bf16 v[50:65], v[118:121], v[110:113], v[50:65]
	v_mfma_f32_32x32x16_bf16 v[18:33], v[122:125], v[110:113], v[18:33]
	v_mfma_f32_32x32x16_bf16 v[82:97], v[126:129], v[110:113], v[82:97]
	s_waitcnt lgkmcnt(6)
	v_mfma_f32_32x32x16_bf16 v[2:17], v[110:113], v[174:177], v[2:17]
	v_or_b32_e32 v118, 28, v214
	v_or_b32_e32 v110, v118, v215
	v_ashrrev_i32_e32 v111, 31, v110
	v_or_b32_e32 v112, v118, v216
	v_lshlrev_b64 v[110:111], 10, v[110:111]
	v_ashrrev_i32_e32 v113, 31, v112
	v_lshl_add_u64 v[110:111], v[202:203], 0, v[110:111]
	v_lshlrev_b64 v[112:113], 10, v[112:113]
	v_lshl_add_u64 v[112:113], v[202:203], 0, v[112:113]
	global_load_dwordx4 v[174:177], v[110:111], off
	global_load_dwordx4 v[182:185], v[112:113], off
	v_or_b32_e32 v110, v118, v217
	v_ashrrev_i32_e32 v111, 31, v110
	v_lshlrev_b64 v[110:111], 10, v[110:111]
	v_lshl_add_u64 v[110:111], v[202:203], 0, v[110:111]
	global_load_dwordx4 v[186:189], v[110:111], off
	s_waitcnt vmcnt(16)
	ds_write_b128 v208, v[150:153] offset:49152
	s_waitcnt vmcnt(15)
	ds_write_b128 v208, v[166:169] offset:57344
	s_waitcnt vmcnt(14)
	ds_write_b128 v209, v[178:181]
	ds_read_b128 v[110:113], v206 offset:25600
	ds_read_b128 v[118:121], v206 offset:29696
	ds_read_b128 v[122:125], v206 offset:33792
	ds_read_b128 v[126:129], v206 offset:37888
	ds_read_b128 v[150:153], v206 offset:41984
	ds_read_b128 v[166:169], v206 offset:46080
	s_waitcnt lgkmcnt(14)
	v_mfma_f32_32x32x16_bf16 v[50:65], v[114:117], v[158:161], v[50:65]
	s_waitcnt lgkmcnt(13)
	v_mfma_f32_32x32x16_bf16 v[18:33], v[218:221], v[158:161], v[18:33]
	s_waitcnt lgkmcnt(12)
	v_mfma_f32_32x32x16_bf16 v[82:97], v[222:225], v[158:161], v[82:97]
	s_waitcnt lgkmcnt(11)
	v_mfma_f32_32x32x16_bf16 v[34:49], v[226:229], v[158:161], v[34:49]
	s_waitcnt lgkmcnt(10)
	v_mfma_f32_32x32x16_bf16 v[66:81], v[158:161], v[230:233], v[66:81]
	s_waitcnt lgkmcnt(9)
	v_mfma_f32_32x32x16_bf16 v[2:17], v[158:161], v[234:237], v[2:17]
	ds_read_b128 v[114:117], v206 offset:26624
	ds_read_b128 v[158:161], v206 offset:30720
	ds_read_b128 v[178:181], v206 offset:34816
	ds_read_b128 v[218:221], v206 offset:38912
	ds_read_b128 v[222:225], v206 offset:43008
	ds_read_b128 v[226:229], v206 offset:47104
	s_waitcnt lgkmcnt(11)
	v_mfma_f32_32x32x16_bf16 v[50:65], v[110:113], v[106:109], v[50:65]
	s_waitcnt lgkmcnt(10)
	v_mfma_f32_32x32x16_bf16 v[18:33], v[118:121], v[106:109], v[18:33]
	s_waitcnt lgkmcnt(9)
	v_mfma_f32_32x32x16_bf16 v[82:97], v[122:125], v[106:109], v[82:97]
	s_waitcnt lgkmcnt(8)
	v_mfma_f32_32x32x16_bf16 v[34:49], v[126:129], v[106:109], v[34:49]
	s_waitcnt lgkmcnt(7)
	v_mfma_f32_32x32x16_bf16 v[66:81], v[106:109], v[150:153], v[66:81]
	s_waitcnt lgkmcnt(6)
	v_mfma_f32_32x32x16_bf16 v[2:17], v[106:109], v[166:169], v[2:17]
	s_waitcnt lgkmcnt(6)
	s_barrier
	ds_read_b128 v[106:109], v206 offset:27648
	ds_read_b128 v[110:113], v206 offset:31744
	ds_read_b128 v[118:121], v206 offset:35840
	ds_read_b128 v[122:125], v206 offset:39936
	ds_read_b128 v[126:129], v206 offset:44032
	ds_read_b128 v[230:233], v206 offset:48128
	s_waitcnt lgkmcnt(11)
	v_mfma_f32_32x32x16_bf16 v[50:65], v[114:117], v[102:105], v[50:65]
	s_waitcnt lgkmcnt(10)
	v_mfma_f32_32x32x16_bf16 v[18:33], v[158:161], v[102:105], v[18:33]
	s_waitcnt lgkmcnt(9)
	v_mfma_f32_32x32x16_bf16 v[82:97], v[178:181], v[102:105], v[82:97]
	s_waitcnt lgkmcnt(8)
	v_mfma_f32_32x32x16_bf16 v[34:49], v[218:221], v[102:105], v[34:49]
	s_waitcnt lgkmcnt(7)
	v_mfma_f32_32x32x16_bf16 v[66:81], v[102:105], v[222:225], v[66:81]
	s_waitcnt lgkmcnt(6)
	v_mfma_f32_32x32x16_bf16 v[2:17], v[102:105], v[226:229], v[2:17]
	ds_read_b128 v[102:105], v206 offset:49152
	ds_read_b128 v[114:117], v206 offset:53248
	ds_read_b128 v[218:221], v206 offset:57344
	ds_read_b128 v[222:225], v206 offset:61440
	ds_read_b128 v[226:229], v244
	ds_read_b128 v[234:237], v240
	s_waitcnt lgkmcnt(11)
	v_mfma_f32_32x32x16_bf16 v[50:65], v[106:109], v[98:101], v[50:65]
	v_add_co_u32_e32 v106, vcc, s33, v204
	s_nop 1
	v_addc_co_u32_e32 v107, vcc, 0, v205, vcc
	global_load_dwordx4 v[178:181], v[106:107], off
	global_load_dwordx4 v[166:169], v[106:107], off offset:1024
	global_load_dwordx4 v[158:161], v[106:107], off offset:2048
	global_load_dwordx4 v[150:153], v[106:107], off offset:3072
	s_waitcnt lgkmcnt(10)
	v_mfma_f32_32x32x16_bf16 v[18:33], v[110:113], v[98:101], v[18:33]
	s_waitcnt lgkmcnt(9)
	v_mfma_f32_32x32x16_bf16 v[82:97], v[118:121], v[98:101], v[82:97]
	s_waitcnt lgkmcnt(8)
	v_mfma_f32_32x32x16_bf16 v[34:49], v[122:125], v[98:101], v[34:49]
	s_waitcnt lgkmcnt(7)
	v_mfma_f32_32x32x16_bf16 v[66:81], v[98:101], v[126:129], v[66:81]
	s_waitcnt lgkmcnt(6)
	v_mfma_f32_32x32x16_bf16 v[2:17], v[98:101], v[230:233], v[2:17]
	s_waitcnt vmcnt(13)
	ds_write_b128 v208, v[190:193]
	s_waitcnt vmcnt(12)
	ds_write_b128 v208, v[194:197] offset:8192
	s_waitcnt vmcnt(11)
	ds_write_b128 v208, v[198:201] offset:16384
	ds_read_b128 v[98:101], v206 offset:50176
	ds_read_b128 v[106:109], v206 offset:54272
	ds_read_b128 v[110:113], v206 offset:58368
	ds_read_b128 v[118:121], v206 offset:62464
	ds_read_b128 v[122:125], v241
	ds_read_b128 v[126:129], v242
	s_waitcnt lgkmcnt(14)
	v_mfma_f32_32x32x16_bf16 v[50:65], v[102:105], v[142:145], v[50:65]
	s_waitcnt lgkmcnt(13)
	v_mfma_f32_32x32x16_bf16 v[18:33], v[114:117], v[142:145], v[18:33]
	s_waitcnt lgkmcnt(12)
	v_mfma_f32_32x32x16_bf16 v[82:97], v[218:221], v[142:145], v[82:97]
	s_waitcnt lgkmcnt(11)
	v_mfma_f32_32x32x16_bf16 v[34:49], v[222:225], v[142:145], v[34:49]
	s_waitcnt lgkmcnt(10)
	v_mfma_f32_32x32x16_bf16 v[66:81], v[142:145], v[226:229], v[66:81]
	s_waitcnt lgkmcnt(9)
	v_mfma_f32_32x32x16_bf16 v[2:17], v[142:145], v[234:237], v[2:17]
	ds_read_b128 v[102:105], v206 offset:51200
	ds_read_b128 v[114:117], v206 offset:55296
	ds_read_b128 v[218:221], v206 offset:59392
	ds_read_b128 v[222:225], v206 offset:63488
	ds_read_b128 v[226:229], v243
	ds_read_b128 v[230:233], v245
	s_waitcnt lgkmcnt(11)
	v_mfma_f32_32x32x16_bf16 v[50:65], v[98:101], v[138:141], v[50:65]
	s_waitcnt lgkmcnt(10)
	v_mfma_f32_32x32x16_bf16 v[18:33], v[106:109], v[138:141], v[18:33]
	s_waitcnt lgkmcnt(9)
	v_mfma_f32_32x32x16_bf16 v[82:97], v[110:113], v[138:141], v[82:97]
	s_waitcnt lgkmcnt(8)
	v_mfma_f32_32x32x16_bf16 v[34:49], v[118:121], v[138:141], v[34:49]
	s_waitcnt lgkmcnt(7)
	v_mfma_f32_32x32x16_bf16 v[66:81], v[138:141], v[122:125], v[66:81]
	s_waitcnt lgkmcnt(6)
	v_mfma_f32_32x32x16_bf16 v[2:17], v[138:141], v[126:129], v[2:17]
	s_waitcnt lgkmcnt(6)
	s_barrier
	ds_read_b128 v[98:101], v206 offset:52224
	ds_read_b128 v[106:109], v206 offset:56320
	ds_read_b128 v[110:113], v206 offset:60416
	ds_read_b128 v[118:121], v206 offset:64512
	ds_read_b128 v[122:125], v246
	ds_read_b128 v[126:129], v247
	s_waitcnt lgkmcnt(11)
	v_mfma_f32_32x32x16_bf16 v[50:65], v[102:105], v[134:137], v[50:65]
	s_waitcnt lgkmcnt(10)
	v_mfma_f32_32x32x16_bf16 v[18:33], v[114:117], v[134:137], v[18:33]
	s_waitcnt lgkmcnt(9)
	v_mfma_f32_32x32x16_bf16 v[82:97], v[218:221], v[134:137], v[82:97]
	s_waitcnt lgkmcnt(8)
	v_mfma_f32_32x32x16_bf16 v[34:49], v[222:225], v[134:137], v[34:49]
	s_waitcnt lgkmcnt(7)
	v_mfma_f32_32x32x16_bf16 v[66:81], v[134:137], v[226:229], v[66:81]
	s_waitcnt lgkmcnt(6)
	v_mfma_f32_32x32x16_bf16 v[2:17], v[134:137], v[230:233], v[2:17]
	ds_read_b128 v[102:105], v206
	ds_read_b128 v[114:117], v206 offset:4096
	ds_read_b128 v[218:221], v206 offset:8192
	ds_read_b128 v[222:225], v206 offset:12288
	ds_read_b128 v[226:229], v206 offset:16384
	ds_read_b128 v[230:233], v206 offset:20480
	s_waitcnt lgkmcnt(11)
	v_mfma_f32_32x32x16_bf16 v[50:65], v[98:101], v[130:133], v[50:65]
	s_waitcnt lgkmcnt(10)
	v_mfma_f32_32x32x16_bf16 v[18:33], v[106:109], v[130:133], v[18:33]
	s_waitcnt lgkmcnt(9)
	v_mfma_f32_32x32x16_bf16 v[82:97], v[110:113], v[130:133], v[82:97]
	s_waitcnt lgkmcnt(8)
	v_mfma_f32_32x32x16_bf16 v[34:49], v[118:121], v[130:133], v[34:49]
	s_waitcnt lgkmcnt(7)
	v_mfma_f32_32x32x16_bf16 v[66:81], v[130:133], v[122:125], v[66:81]
	s_waitcnt lgkmcnt(6)
	v_mfma_f32_32x32x16_bf16 v[2:17], v[130:133], v[126:129], v[2:17]
	s_waitcnt vmcnt(6)
	ds_write_b128 v208, v[174:177] offset:24576
	s_waitcnt vmcnt(5)
	ds_write_b128 v208, v[182:185] offset:32768
	s_waitcnt vmcnt(4)
	ds_write_b128 v208, v[186:189] offset:40960
	s_lshl_b64 s[42:43], s[2:3], 9
	s_or_b64 s[42:43], s[42:43], s[6:7]
	v_or_b32_e32 v252, s42, v211
	v_lshlrev_b32_e32 v252, 8, v252
	v_lshl_or_b32 v252, v212, 5, v252
	v_or_b32_e32 v252, v252, v1
	v_lshlrev_b32_e32 v252, 2, v252
	global_load_dword v249, v252, s[8:9]
	global_load_dword v248, v252, s[8:9] offset:1024
	global_load_dword v247, v252, s[8:9] offset:2048
	global_load_dword v246, v252, s[8:9] offset:3072
	global_load_dword v245, v252, s[44:45]
	global_load_dword v243, v252, s[44:45] offset:1024
	global_load_dword v241, v252, s[44:45] offset:2048
	global_load_dword v239, v252, s[44:45] offset:3072
	global_load_dword v244, v252, s[46:47]
	global_load_dword v242, v252, s[46:47] offset:1024
	global_load_dword v240, v252, s[46:47] offset:2048
	global_load_dword v238, v252, s[46:47] offset:3072
	global_load_dword v236, v252, s[48:49]
	global_load_dword v234, v252, s[48:49] offset:1024
	global_load_dword v237, v252, s[50:51]
	global_load_dword v235, v252, s[50:51] offset:1024
	ds_read_b128 v[98:101], v206 offset:1024
	ds_read_b128 v[106:109], v206 offset:5120
	ds_read_b128 v[110:113], v206 offset:9216
	ds_read_b128 v[118:121], v206 offset:13312
	ds_read_b128 v[122:125], v206 offset:17408
	ds_read_b128 v[126:129], v206 offset:21504
	s_waitcnt lgkmcnt(14)
	v_mfma_f32_32x32x16_bf16 v[50:65], v[102:105], v[170:173], v[50:65]
	s_waitcnt lgkmcnt(13)
	v_mfma_f32_32x32x16_bf16 v[18:33], v[114:117], v[170:173], v[18:33]
	s_waitcnt lgkmcnt(12)
	v_mfma_f32_32x32x16_bf16 v[82:97], v[218:221], v[170:173], v[82:97]
	s_waitcnt lgkmcnt(11)
	v_mfma_f32_32x32x16_bf16 v[34:49], v[222:225], v[170:173], v[34:49]
	s_waitcnt lgkmcnt(10)
	v_mfma_f32_32x32x16_bf16 v[66:81], v[170:173], v[226:229], v[66:81]
	s_waitcnt lgkmcnt(9)
	v_mfma_f32_32x32x16_bf16 v[2:17], v[170:173], v[230:233], v[2:17]
	ds_read_b128 v[102:105], v206 offset:2048
	ds_read_b128 v[114:117], v206 offset:6144
	ds_read_b128 v[218:221], v206 offset:10240
	ds_read_b128 v[222:225], v206 offset:14336
	ds_read_b128 v[226:229], v206 offset:18432
	ds_read_b128 v[230:233], v206 offset:22528
	s_waitcnt lgkmcnt(11)
	v_mfma_f32_32x32x16_bf16 v[50:65], v[98:101], v[162:165], v[50:65]
	s_waitcnt lgkmcnt(10)
	v_mfma_f32_32x32x16_bf16 v[18:33], v[106:109], v[162:165], v[18:33]
	s_waitcnt lgkmcnt(9)
	v_mfma_f32_32x32x16_bf16 v[82:97], v[110:113], v[162:165], v[82:97]
	s_waitcnt lgkmcnt(8)
	v_mfma_f32_32x32x16_bf16 v[34:49], v[118:121], v[162:165], v[34:49]
	s_waitcnt lgkmcnt(7)
	v_mfma_f32_32x32x16_bf16 v[66:81], v[162:165], v[122:125], v[66:81]
	s_waitcnt lgkmcnt(6)
	v_mfma_f32_32x32x16_bf16 v[2:17], v[162:165], v[126:129], v[2:17]
	s_waitcnt lgkmcnt(6)
	s_barrier
	ds_read_b128 v[98:101], v206 offset:3072
	ds_read_b128 v[106:109], v206 offset:7168
	ds_read_b128 v[110:113], v206 offset:11264
	ds_read_b128 v[118:121], v206 offset:15360
	ds_read_b128 v[122:125], v206 offset:19456
	ds_read_b128 v[126:129], v206 offset:23552
	s_waitcnt lgkmcnt(11)
	v_mfma_f32_32x32x16_bf16 v[50:65], v[102:105], v[154:157], v[50:65]
	s_waitcnt lgkmcnt(10)
	v_mfma_f32_32x32x16_bf16 v[18:33], v[114:117], v[154:157], v[18:33]
	s_waitcnt lgkmcnt(9)
	v_mfma_f32_32x32x16_bf16 v[82:97], v[218:221], v[154:157], v[82:97]
	s_waitcnt lgkmcnt(8)
	v_mfma_f32_32x32x16_bf16 v[34:49], v[222:225], v[154:157], v[34:49]
	s_waitcnt lgkmcnt(7)
	v_mfma_f32_32x32x16_bf16 v[66:81], v[154:157], v[226:229], v[66:81]
	s_waitcnt lgkmcnt(6)
	v_mfma_f32_32x32x16_bf16 v[2:17], v[154:157], v[230:233], v[2:17]
	ds_read_b128 v[102:105], v206 offset:24576
	ds_read_b128 v[114:117], v206 offset:28672
	ds_read_b128 v[218:221], v206 offset:32768
	ds_read_b128 v[222:225], v206 offset:36864
	ds_read_b128 v[226:229], v206 offset:40960
	ds_read_b128 v[230:233], v206 offset:45056
	s_waitcnt lgkmcnt(11)
	v_mfma_f32_32x32x16_bf16 v[50:65], v[98:101], v[146:149], v[50:65]
	s_waitcnt lgkmcnt(10)
	v_mfma_f32_32x32x16_bf16 v[18:33], v[106:109], v[146:149], v[18:33]
	s_waitcnt lgkmcnt(9)
	v_mfma_f32_32x32x16_bf16 v[82:97], v[110:113], v[146:149], v[82:97]
	s_waitcnt lgkmcnt(8)
	v_mfma_f32_32x32x16_bf16 v[34:49], v[118:121], v[146:149], v[34:49]
	s_waitcnt lgkmcnt(7)
	v_mfma_f32_32x32x16_bf16 v[66:81], v[146:149], v[122:125], v[66:81]
	s_waitcnt lgkmcnt(6)
	v_mfma_f32_32x32x16_bf16 v[2:17], v[146:149], v[126:129], v[2:17]
	ds_read_b128 v[98:101], v206 offset:25600
	ds_read_b128 v[106:109], v206 offset:29696
	ds_read_b128 v[110:113], v206 offset:33792
	ds_read_b128 v[118:121], v206 offset:37888
	ds_read_b128 v[122:125], v206 offset:41984
	ds_read_b128 v[126:129], v206 offset:46080
	s_waitcnt vmcnt(19) lgkmcnt(11)
	v_mfma_f32_32x32x16_bf16 v[50:65], v[102:105], v[178:181], v[50:65]
	s_waitcnt lgkmcnt(10)
	v_mfma_f32_32x32x16_bf16 v[18:33], v[114:117], v[178:181], v[18:33]
	s_waitcnt lgkmcnt(9)
	v_mfma_f32_32x32x16_bf16 v[82:97], v[218:221], v[178:181], v[82:97]
	s_waitcnt lgkmcnt(8)
	v_mfma_f32_32x32x16_bf16 v[34:49], v[222:225], v[178:181], v[34:49]
	s_waitcnt lgkmcnt(7)
	v_mfma_f32_32x32x16_bf16 v[66:81], v[178:181], v[226:229], v[66:81]
	s_waitcnt lgkmcnt(6)
	v_mfma_f32_32x32x16_bf16 v[2:17], v[178:181], v[230:233], v[2:17]
	ds_read_b128 v[102:105], v206 offset:26624
	ds_read_b128 v[114:117], v206 offset:30720
	ds_read_b128 v[218:221], v206 offset:34816
	ds_read_b128 v[222:225], v206 offset:38912
	ds_read_b128 v[226:229], v206 offset:43008
	ds_read_b128 v[230:233], v206 offset:47104
	s_waitcnt vmcnt(18) lgkmcnt(11)
	v_mfma_f32_32x32x16_bf16 v[50:65], v[98:101], v[166:169], v[50:65]
	s_waitcnt lgkmcnt(10)
	v_mfma_f32_32x32x16_bf16 v[18:33], v[106:109], v[166:169], v[18:33]
	s_waitcnt lgkmcnt(9)
	v_mfma_f32_32x32x16_bf16 v[82:97], v[110:113], v[166:169], v[82:97]
	s_waitcnt lgkmcnt(8)
	v_mfma_f32_32x32x16_bf16 v[34:49], v[118:121], v[166:169], v[34:49]
	s_waitcnt lgkmcnt(7)
	v_mfma_f32_32x32x16_bf16 v[66:81], v[166:169], v[122:125], v[66:81]
	s_waitcnt lgkmcnt(6)
	v_mfma_f32_32x32x16_bf16 v[2:17], v[166:169], v[126:129], v[2:17]
	s_waitcnt lgkmcnt(6)
	s_barrier
	ds_read_b128 v[98:101], v206 offset:27648
	ds_read_b128 v[106:109], v206 offset:31744
	ds_read_b128 v[110:113], v206 offset:35840
	ds_read_b128 v[118:121], v206 offset:39936
	ds_read_b128 v[122:125], v206 offset:44032
	ds_read_b128 v[126:129], v206 offset:48128
	s_waitcnt vmcnt(17) lgkmcnt(11)
	v_mfma_f32_32x32x16_bf16 v[50:65], v[102:105], v[158:161], v[50:65]
	s_waitcnt lgkmcnt(10)
	v_mfma_f32_32x32x16_bf16 v[18:33], v[114:117], v[158:161], v[18:33]
	s_waitcnt lgkmcnt(9)
	v_mfma_f32_32x32x16_bf16 v[82:97], v[218:221], v[158:161], v[82:97]
	s_waitcnt lgkmcnt(8)
	v_mfma_f32_32x32x16_bf16 v[34:49], v[222:225], v[158:161], v[34:49]
	s_waitcnt lgkmcnt(7)
	v_mfma_f32_32x32x16_bf16 v[66:81], v[158:161], v[226:229], v[66:81]
	s_waitcnt lgkmcnt(6)
	v_mfma_f32_32x32x16_bf16 v[2:17], v[158:161], v[230:233], v[2:17]
	global_load_dword v232, v252, s[48:49] offset:2048
	global_load_dword v230, v252, s[48:49] offset:3072
	global_load_dword v233, v252, s[50:51] offset:2048
	global_load_dword v231, v252, s[50:51] offset:3072
	global_load_dword v228, v252, s[52:53]
	global_load_dword v226, v252, s[52:53] offset:1024
	global_load_dword v224, v252, s[52:53] offset:2048
	global_load_dword v222, v252, s[52:53] offset:3072
	global_load_dword v229, v252, s[54:55]
	global_load_dword v227, v252, s[54:55] offset:1024
	global_load_dword v225, v252, s[54:55] offset:2048
	global_load_dword v223, v252, s[54:55] offset:3072
	global_load_dword v221, v252, s[56:57]
	global_load_dword v220, v252, s[56:57] offset:1024
	global_load_dword v219, v252, s[56:57] offset:2048
	global_load_dword v218, v252, s[56:57] offset:3072
	s_waitcnt vmcnt(32) lgkmcnt(5)
	v_mfma_f32_32x32x16_bf16 v[50:65], v[98:101], v[150:153], v[50:65]
	s_waitcnt lgkmcnt(4)
	v_mfma_f32_32x32x16_bf16 v[18:33], v[106:109], v[150:153], v[18:33]
	s_waitcnt lgkmcnt(3)
	v_mfma_f32_32x32x16_bf16 v[82:97], v[110:113], v[150:153], v[82:97]
	s_waitcnt lgkmcnt(2)
	v_mfma_f32_32x32x16_bf16 v[34:49], v[118:121], v[150:153], v[34:49]
	s_waitcnt lgkmcnt(1)
	v_mfma_f32_32x32x16_bf16 v[66:81], v[150:153], v[122:125], v[66:81]
	s_waitcnt lgkmcnt(0)
	v_mfma_f32_32x32x16_bf16 v[2:17], v[150:153], v[126:129], v[2:17]
	s_barrier
	s_and_b64 vcc, exec, s[18:19]
	s_cbranch_vccnz .LBB3_141
	v_or_b32_e32 v100, v215, v214
	v_ashrrev_i32_e32 v101, 31, v100
	v_or_b32_e32 v102, v216, v214
	v_lshlrev_b64 v[100:101], 10, v[100:101]
	v_ashrrev_i32_e32 v103, 31, v102
	v_lshl_add_u64 v[100:101], v[202:203], 0, v[100:101]
	v_lshlrev_b64 v[102:103], 10, v[102:103]
	v_lshl_add_u64 v[102:103], v[202:203], 0, v[102:103]
	global_load_dwordx4 v[190:193], v[100:101], off
	global_load_dwordx4 v[194:197], v[102:103], off
	v_or_b32_e32 v100, v217, v214
	v_or_b32_e32 v104, 4, v214
	v_ashrrev_i32_e32 v101, 31, v100
	v_or_b32_e32 v102, v104, v215
	v_lshlrev_b64 v[100:101], 10, v[100:101]
	v_ashrrev_i32_e32 v103, 31, v102
	v_add_u32_e32 v98, s28, v212
	v_lshl_add_u64 v[100:101], v[202:203], 0, v[100:101]
	v_lshlrev_b64 v[102:103], 10, v[102:103]
	v_ashrrev_i32_e32 v99, 31, v98
	v_lshl_add_u64 v[102:103], v[202:203], 0, v[102:103]
	global_load_dwordx4 v[198:201], v[100:101], off
	global_load_dwordx4 v[174:177], v[102:103], off
	v_or_b32_e32 v100, v216, v104
	v_lshlrev_b64 v[98:99], 15, v[98:99]
	v_ashrrev_i32_e32 v101, 31, v100
	v_or_b32_e32 v102, v217, v104
	v_lshl_add_u64 v[98:99], s[10:11], 0, v[98:99]
	v_lshlrev_b64 v[100:101], 10, v[100:101]
	v_ashrrev_i32_e32 v103, 31, v102
	v_lshl_add_u64 v[98:99], v[98:99], 0, v[206:207]
	v_lshl_add_u64 v[100:101], v[202:203], 0, v[100:101]
	v_lshlrev_b64 v[102:103], 10, v[102:103]
	v_lshl_add_u64 v[102:103], v[202:203], 0, v[102:103]
	global_load_dwordx4 v[182:185], v[100:101], off
	global_load_dwordx4 v[186:189], v[102:103], off
	global_load_dwordx4 v[170:173], v[98:99], off
	global_load_dwordx4 v[162:165], v[98:99], off offset:1024
	global_load_dwordx4 v[154:157], v[98:99], off offset:2048
	global_load_dwordx4 v[146:149], v[98:99], off offset:3072
	v_add_co_u32_e32 v100, vcc, 0x1000, v98
	s_nop 1
	v_addc_co_u32_e32 v101, vcc, 0, v99, vcc
	v_add_co_u32_e32 v98, vcc, 0x2000, v98
	global_load_dwordx4 v[178:181], v[100:101], off
	global_load_dwordx4 v[166:169], v[100:101], off offset:1024
	global_load_dwordx4 v[158:161], v[100:101], off offset:2048
	global_load_dwordx4 v[150:153], v[100:101], off offset:3072
	v_addc_co_u32_e32 v99, vcc, 0, v99, vcc
	global_load_dwordx4 v[142:145], v[98:99], off
	global_load_dwordx4 v[138:141], v[98:99], off offset:1024
	global_load_dwordx4 v[134:137], v[98:99], off offset:2048
	global_load_dwordx4 v[130:133], v[98:99], off offset:3072
	s_branch .LBB3_141
